# conversion loops in P1 queue, P3 and P4 fills: loop-head wait leaves the previous tile's stores outstanding
# speedup vs baseline: 1.0070x; 1.0023x over previous
; #define LAS __attribute__((address_space(3)))
; __device__ __forceinline__ void conv8b_run(const Ctx& X, int first, int step, int count) {
;     if (count <= 0) return;
;     f32x4 v[16];
;     Cvb c = conv8b_dec(X, first), cn = c;
; #pragma unroll
;     for (int i = 0; i < 16; ++i) v[i] = __builtin_nontemporal_load((const f32x4*)(c.W + (size_t)i * c.N));
; __device__ __forceinline__ void conv8_queue(const Ctx& X, int n) {
;     LAS int* qw = (LAS int*)(X.lds + LDS_MISC + 64);
;     unsigned zo = 0; asm volatile("" : "+v"(zo));
;     int nb_ = 0;
;     if (X.tid == 0) nb_ = (int)__hip_atomic_fetch_add(XP_ctl(X) + CW_WQ + zo, (unsigned)(8 * CQ_CHUNK), __ATOMIC_RELAXED, __HIP_MEMORY_SCOPE_AGENT);
;     for (;;) {
;         if (X.tid == 0) *qw = nb_;
;         __syncthreads();
;         const int base = __builtin_amdgcn_readfirstlane(*qw);
;         if (base >= n) break;
;         if (X.tid == 0) nb_ = (int)__hip_atomic_fetch_add(XP_ctl(X) + CW_WQ + zo, (unsigned)(8 * CQ_CHUNK), __ATOMIC_RELAXED, __HIP_MEMORY_SCOPE_AGENT);
;         const int left = (n - base) >> 3;
;         conv8b_run(X, base >> 3, 1, left < CQ_CHUNK ? left : CQ_CHUNK);
.LBB0_138:
	s_min_i32 s23, s23, 2
	s_add_u32 s12, s12, s6
	s_addc_u32 s13, s13, 0
	s_lshl_b32 s11, s25, 7
	s_add_i32 s11, s11, s19
	s_mul_hi_u32 s25, s10, s11
	s_mul_i32 s24, s10, s11
	s_lshl_b32 s6, s26, 8
	s_lshl_b64 s[24:25], s[24:25], 2
	s_add_u32 s11, s8, s24
	s_addc_u32 s24, s9, s25
	s_lshl_b64 s[8:9], s[6:7], 2
	s_add_u32 s8, s11, s8
	s_addc_u32 s9, s24, s9
	v_add_u32_e32 v72, s6, v77
	v_lshl_add_u64 v[2:3], s[8:9], 0, v[66:67]
	s_mul_i32 s6, s10, 60
	v_lshl_add_u64 v[2:3], v[2:3], 0, s[6:7]
	s_lshl_b32 s6, s10, 2
	s_sub_u32 s10, 0, s6
	s_subb_u32 s11, 0, 0
	v_lshl_add_u64 v[4:5], v[2:3], 0, s[10:11]
	global_load_dwordx4 v[18:21], v[2:3], off nt
	global_load_dwordx4 v[10:13], v[4:5], off nt
	v_lshl_add_u64 v[2:3], v[4:5], 0, s[10:11]
	v_lshl_add_u64 v[4:5], v[2:3], 0, s[10:11]
	global_load_dwordx4 v[34:37], v[2:3], off nt
	global_load_dwordx4 v[26:29], v[4:5], off nt
	v_lshl_add_u64 v[2:3], v[4:5], 0, s[10:11]
	v_lshl_add_u64 v[4:5], v[2:3], 0, s[10:11]
	global_load_dwordx4 v[62:65], v[2:3], off nt
	global_load_dwordx4 v[42:45], v[4:5], off nt
	v_lshl_add_u64 v[2:3], v[4:5], 0, s[10:11]
	global_load_dwordx4 v[58:61], v[2:3], off nt
	v_lshl_add_u64 v[2:3], v[2:3], 0, s[10:11]
	global_load_dwordx4 v[54:57], v[2:3], off nt
	v_lshl_add_u64 v[2:3], v[2:3], 0, s[10:11]
	global_load_dwordx4 v[50:53], v[2:3], off nt
	v_lshl_add_u64 v[2:3], v[2:3], 0, s[10:11]
	global_load_dwordx4 v[38:41], v[2:3], off nt
	v_lshl_add_u64 v[2:3], v[2:3], 0, s[10:11]
	global_load_dwordx4 v[46:49], v[2:3], off nt
	v_lshl_add_u64 v[2:3], v[2:3], 0, s[10:11]
	global_load_dwordx4 v[22:25], v[2:3], off nt
	v_lshl_add_u64 v[2:3], v[2:3], 0, s[10:11]
	global_load_dwordx4 v[30:33], v[2:3], off nt
	v_lshl_add_u64 v[2:3], v[2:3], 0, s[10:11]
	v_lshl_add_u64 v[74:75], v[2:3], 0, s[10:11]
	global_load_dwordx4 v[6:9], v[2:3], off nt
	global_load_dwordx4 v[14:17], v[74:75], off nt
	s_nop 0
	global_load_dwordx4 v[2:5], v66, s[8:9] nt
	v_mov_b32_e32 v73, v67
	v_lshlrev_b64 v[72:73], 7, v[72:73]
	v_lshl_add_u64 v[72:73], s[12:13], 0, v[72:73]
	v_lshl_add_u64 v[72:73], v[72:73], 0, v[70:71]
	s_mov_b32 s6, 0
	v_mov_b64_e32 v[74:75], v[72:73]
	s_waitcnt vmcnt(0)
	s_branch .LBB0_141

; #define LAS __attribute__((address_space(3)))
; __device__ __forceinline__ void conv8b_run(const Ctx& X, int first, int step, int count) {
;     ...
;         LAS uchar* buf = X.lds + (j & 1) * CVT_BUF;
; #pragma unroll
;         for (int q = 0; q < 4; ++q) { u32x4 o;
;             o.x = pk_fp8x4(v[0][q] * W8_SCALE, v[1][q] * W8_SCALE, v[2][q] * W8_SCALE, v[3][q] * W8_SCALE); o.y = pk_fp8x4(v[4][q] * W8_SCALE, v[5][q] * W8_SCALE, v[6][q] * W8_SCALE, v[7][q] * W8_SCALE);
;             o.z = pk_fp8x4(v[8][q] * W8_SCALE, v[9][q] * W8_SCALE, v[10][q] * W8_SCALE, v[11][q] * W8_SCALE); o.w = pk_fp8x4(v[12][q] * W8_SCALE, v[13][q] * W8_SCALE, v[14][q] * W8_SCALE, v[15][q] * W8_SCALE);
;             *(LAS u32x4*)(buf + (4 * X.lane + q) * CVT_STRIDE + 16 * X.wave) = o; }
;         if (j + 1 < count) { cn = conv8b_dec(X, first + (j + 1) * step);
; #pragma unroll
;             for (int i = 0; i < 16; ++i) v[i] = __builtin_nontemporal_load((const f32x4*)(cn.W + (size_t)i * cn.N)); }
.LBB0_141:
	s_waitcnt vmcnt(4)
	v_mul_f32_e32 v83, 0x42800000, v2
	v_mul_f32_e32 v84, 0x42800000, v14
	v_med3_f32 v83, v83, s21, v82
	v_med3_f32 v86, v84, s21, v82
	v_mov_b32_e32 v84, 0
	v_cvt_pk_fp8_f32 v84, v83, v86
	v_mul_f32_e32 v85, 0x42800000, v6
	v_mul_f32_e32 v83, 0x42800000, v30
	v_med3_f32 v85, v85, s21, v82
	v_med3_f32 v83, v83, s21, v82
	v_cvt_pk_fp8_f32 v84, v85, v83 op_sel:[0,0,1]
	v_mul_f32_e32 v83, 0x42800000, v22
	v_mul_f32_e32 v85, 0x42800000, v46
	v_med3_f32 v83, v83, s21, v82
	v_med3_f32 v87, v85, s21, v82
	v_mov_b32_e32 v85, 0
	v_cvt_pk_fp8_f32 v85, v83, v87
	v_mul_f32_e32 v86, 0x42800000, v38
	v_mul_f32_e32 v83, 0x42800000, v50
	v_med3_f32 v86, v86, s21, v82
	v_med3_f32 v83, v83, s21, v82
	v_cvt_pk_fp8_f32 v85, v86, v83 op_sel:[0,0,1]
	v_mul_f32_e32 v83, 0x42800000, v54
	v_mul_f32_e32 v86, 0x42800000, v58
	v_med3_f32 v83, v83, s21, v82
	v_med3_f32 v88, v86, s21, v82
	v_mov_b32_e32 v86, 0
	v_cvt_pk_fp8_f32 v86, v83, v88
	v_mul_f32_e32 v87, 0x42800000, v42
	v_mul_f32_e32 v83, 0x42800000, v62
	v_med3_f32 v87, v87, s21, v82
	v_med3_f32 v83, v83, s21, v82
	v_cvt_pk_fp8_f32 v86, v87, v83 op_sel:[0,0,1]
	v_mul_f32_e32 v83, 0x42800000, v26
	v_mul_f32_e32 v87, 0x42800000, v34
	v_med3_f32 v83, v83, s21, v82
	v_med3_f32 v89, v87, s21, v82
	v_mov_b32_e32 v87, 0
	v_cvt_pk_fp8_f32 v87, v83, v89
	v_mul_f32_e32 v88, 0x42800000, v10
	v_mul_f32_e32 v83, 0x42800000, v18
	v_med3_f32 v88, v88, s21, v82
	v_med3_f32 v83, v83, s21, v82
	v_cvt_pk_fp8_f32 v87, v88, v83 op_sel:[0,0,1]
	v_mul_f32_e32 v83, 0x42800000, v3
	v_mul_f32_e32 v88, 0x42800000, v15
	v_med3_f32 v83, v83, s21, v82
	v_med3_f32 v90, v88, s21, v82
	v_mov_b32_e32 v88, 0
	v_cvt_pk_fp8_f32 v88, v83, v90
	v_mul_f32_e32 v89, 0x42800000, v7
	v_mul_f32_e32 v83, 0x42800000, v31
	v_med3_f32 v89, v89, s21, v82
	v_med3_f32 v83, v83, s21, v82
	v_cvt_pk_fp8_f32 v88, v89, v83 op_sel:[0,0,1]
	v_mul_f32_e32 v83, 0x42800000, v23
	v_mul_f32_e32 v89, 0x42800000, v47
	v_med3_f32 v83, v83, s21, v82
	v_med3_f32 v91, v89, s21, v82
	v_mov_b32_e32 v89, 0
	v_cvt_pk_fp8_f32 v89, v83, v91
	v_mul_f32_e32 v90, 0x42800000, v39
	v_mul_f32_e32 v83, 0x42800000, v51
	v_med3_f32 v90, v90, s21, v82
	v_med3_f32 v83, v83, s21, v82
	v_cvt_pk_fp8_f32 v89, v90, v83 op_sel:[0,0,1]
	v_mul_f32_e32 v83, 0x42800000, v55
	v_mul_f32_e32 v90, 0x42800000, v59
	v_med3_f32 v83, v83, s21, v82
	v_med3_f32 v92, v90, s21, v82
	v_mov_b32_e32 v90, 0
	v_cvt_pk_fp8_f32 v90, v83, v92
	v_mul_f32_e32 v91, 0x42800000, v43
	v_mul_f32_e32 v83, 0x42800000, v63
	v_med3_f32 v91, v91, s21, v82
	v_med3_f32 v83, v83, s21, v82
	v_cvt_pk_fp8_f32 v90, v91, v83 op_sel:[0,0,1]
	v_mul_f32_e32 v83, 0x42800000, v27
	v_mul_f32_e32 v91, 0x42800000, v35
	v_med3_f32 v83, v83, s21, v82
	v_med3_f32 v93, v91, s21, v82
	v_mov_b32_e32 v91, 0
	v_cvt_pk_fp8_f32 v91, v83, v93
	s_bitcmp1_b32 s6, 0
	v_mul_f32_e32 v92, 0x42800000, v11
	v_mul_f32_e32 v83, 0x42800000, v19
	s_cselect_b32 s8, 0x9000, 0
	v_med3_f32 v92, v92, s21, v82
	v_med3_f32 v83, v83, s21, v82
	s_add_i32 s24, s8, 0
	v_cvt_pk_fp8_f32 v91, v92, v83 op_sel:[0,0,1]
	s_add_i32 s8, s19, s24
	v_add_u32_e32 v83, s8, v78
	ds_write_b128 v83, v[84:87]
	ds_write_b128 v83, v[88:91] offset:144
	v_mul_f32_e32 v84, 0x42800000, v4
	v_mul_f32_e32 v85, 0x42800000, v16
	v_med3_f32 v87, v84, s21, v82
	v_med3_f32 v85, v85, s21, v82
	v_mov_b32_e32 v84, 0
	v_cvt_pk_fp8_f32 v84, v87, v85
	v_mul_f32_e32 v86, 0x42800000, v8
	v_mul_f32_e32 v85, 0x42800000, v32
	v_med3_f32 v86, v86, s21, v82
	v_med3_f32 v85, v85, s21, v82
	v_cvt_pk_fp8_f32 v84, v86, v85 op_sel:[0,0,1]
	v_mul_f32_e32 v85, 0x42800000, v24
	v_mul_f32_e32 v86, 0x42800000, v48
	v_med3_f32 v88, v85, s21, v82
	v_med3_f32 v86, v86, s21, v82
	v_mov_b32_e32 v85, 0
	v_cvt_pk_fp8_f32 v85, v88, v86
	v_mul_f32_e32 v87, 0x42800000, v40
	v_mul_f32_e32 v86, 0x42800000, v52
	v_med3_f32 v87, v87, s21, v82
	v_med3_f32 v86, v86, s21, v82
	v_cvt_pk_fp8_f32 v85, v87, v86 op_sel:[0,0,1]
	v_mul_f32_e32 v86, 0x42800000, v56
	v_mul_f32_e32 v87, 0x42800000, v60
	v_med3_f32 v89, v86, s21, v82
	v_med3_f32 v87, v87, s21, v82
	v_mov_b32_e32 v86, 0
	v_cvt_pk_fp8_f32 v86, v89, v87
	v_mul_f32_e32 v88, 0x42800000, v44
	v_mul_f32_e32 v87, 0x42800000, v64
	v_med3_f32 v88, v88, s21, v82
	v_med3_f32 v87, v87, s21, v82
	v_cvt_pk_fp8_f32 v86, v88, v87 op_sel:[0,0,1]
	v_mul_f32_e32 v87, 0x42800000, v28
	v_mul_f32_e32 v88, 0x42800000, v36
	v_med3_f32 v90, v87, s21, v82
	v_med3_f32 v88, v88, s21, v82
	v_mov_b32_e32 v87, 0
	v_cvt_pk_fp8_f32 v87, v90, v88
	v_mul_f32_e32 v89, 0x42800000, v12
	v_mul_f32_e32 v88, 0x42800000, v20
	v_med3_f32 v89, v89, s21, v82
	v_med3_f32 v88, v88, s21, v82
	v_cvt_pk_fp8_f32 v87, v89, v88 op_sel:[0,0,1]
	v_mul_f32_e32 v88, 0x42800000, v5
	v_mul_f32_e32 v89, 0x42800000, v17
	v_med3_f32 v91, v88, s21, v82
	v_med3_f32 v89, v89, s21, v82
	v_mov_b32_e32 v88, 0
	v_cvt_pk_fp8_f32 v88, v91, v89
	v_mul_f32_e32 v90, 0x42800000, v9
	v_mul_f32_e32 v89, 0x42800000, v33
	v_med3_f32 v90, v90, s21, v82
	v_med3_f32 v89, v89, s21, v82
	v_cvt_pk_fp8_f32 v88, v90, v89 op_sel:[0,0,1]
	v_mul_f32_e32 v89, 0x42800000, v25
	v_mul_f32_e32 v90, 0x42800000, v49
	v_med3_f32 v92, v89, s21, v82
	v_med3_f32 v90, v90, s21, v82
	v_mov_b32_e32 v89, 0
	v_cvt_pk_fp8_f32 v89, v92, v90
	v_mul_f32_e32 v91, 0x42800000, v41
	v_mul_f32_e32 v90, 0x42800000, v53
	v_med3_f32 v91, v91, s21, v82
	v_med3_f32 v90, v90, s21, v82
	v_cvt_pk_fp8_f32 v89, v91, v90 op_sel:[0,0,1]
	v_mul_f32_e32 v90, 0x42800000, v57
	v_mul_f32_e32 v91, 0x42800000, v61
	v_med3_f32 v93, v90, s21, v82
	v_med3_f32 v91, v91, s21, v82
	v_mov_b32_e32 v90, 0
	v_cvt_pk_fp8_f32 v90, v93, v91
	v_mul_f32_e32 v92, 0x42800000, v45
	v_mul_f32_e32 v91, 0x42800000, v65
	v_med3_f32 v92, v92, s21, v82
	v_med3_f32 v91, v91, s21, v82
	v_cvt_pk_fp8_f32 v90, v92, v91 op_sel:[0,0,1]
	v_mul_f32_e32 v91, 0x42800000, v29
	v_mul_f32_e32 v92, 0x42800000, v37
	v_med3_f32 v94, v91, s21, v82
	v_med3_f32 v92, v92, s21, v82
	v_mov_b32_e32 v91, 0
	v_cvt_pk_fp8_f32 v91, v94, v92
	v_mul_f32_e32 v93, 0x42800000, v13
	v_mul_f32_e32 v92, 0x42800000, v21
	v_med3_f32 v93, v93, s21, v82
	v_med3_f32 v92, v92, s21, v82
	v_cvt_pk_fp8_f32 v91, v93, v92 op_sel:[0,0,1]
	s_add_i32 s25, s6, 1
	s_cmp_ge_i32 s25, s23
	ds_write_b128 v83, v[84:87] offset:288
	ds_write_b128 v83, v[88:91] offset:432
	s_cbranch_scc1 .LBB0_140
	s_add_i32 s29, s22, s6
	s_add_i32 s28, s29, 1
	s_cmpk_gt_i32 s28, 0x1fff
	s_mov_b64 s[12:13], -1
	s_cbranch_scc0 .LBB0_144
	s_load_dwordx2 s[8:9], s[0:1], 0x80
	s_addk_i32 s29, 0xe001
	s_lshr_b32 s6, s29, 7
	s_bfe_u32 s27, s28, 0x40003
	s_and_b32 s26, s28, 7
	s_lshl_b64 s[10:11], s[6:7], 24
	s_waitcnt lgkmcnt(0)
	s_add_u32 s8, s8, s10
	s_addc_u32 s9, s9, s11
	s_lshl_b64 s[10:11], s[6:7], 22
	s_add_u32 s10, s15, s10
	s_addc_u32 s11, s16, s11
	s_lshl_b32 s6, s27, 18
	s_mov_b64 s[12:13], 0

; __device__ __forceinline__ void conv8_fill(const Ctx& X, int base, int rank, int nblk, int n) { conv8b_run(X, (base >> 3) + rank, nblk, n); }
; #define SEAM(k) do { if (IN(k) && IN((k) + 1)) xcd_barrier(bar); } while (0)
; __device__ __forceinline__ Cvb conv8b_dec(const Ctx& X, int bit) { Cvb c; int kb, nb;
;     if (bit < I_GU8 / 8) { const int e = bit >> 8, r = bit & 255; kb = r >> 4; nb = r & 15; c.N = 2 * DFF; c.W = XP_w_gu(X) + (size_t)e * D * (2 * DFF); c.WT = XP_WguT(X) + (size_t)e * 16 * PAN_GU + (size_t)kb * PAN_GU; }
;     else { const int b2 = bit - I_GU8 / 8, e = b2 >> 7, r = b2 & 127; kb = r >> 3; nb = r & 7; c.N = D; c.W = XP_w_d(X) + (size_t)e * DFF * D; c.WT = XP_WdT(X) + (size_t)e * 16 * PAN_D + (size_t)kb * PAN_D; }
;     c.W += (size_t)(kb * 128 + 16 * X.wave) * c.N + nb * 256 + 4 * X.lane;
;     c.WT += (size_t)(nb * 256 + 32 * X.wave + (X.lane >> 3)) * 128 + 16 * (X.lane & 7);
;     return c; }
; __device__ __forceinline__ void conv8b_run(const Ctx& X, int first, int step, int count) {
;     if (count <= 0) return;
;     f32x4 v[16];
;     Cvb c = conv8b_dec(X, first), cn = c;
; #pragma unroll
;     for (int i = 0; i < 16; ++i) v[i] = __builtin_nontemporal_load((const f32x4*)(c.W + (size_t)i * c.N));
; __global__ void __launch_bounds__(NTHR, 2) fwd(Args args) {
;     ...
;         if (X.G == 256 && X.bid >= 128) conv8_fill(X, FILL_B4, X.bid - 128, FILL_W4 / NWAVES, FILL_N4); } SEAM(4);
.LBB0_661:
	s_waitcnt lgkmcnt(0)
	s_cmpk_eq_i32 s92, 0x100
	v_readlane_b32 s87, v248, 9
	s_load_dwordx2 s[94:95], s[0:1], 0xa8
	s_cselect_b64 s[2:3], -1, 0
	s_cmpk_gt_i32 s87, 0x7f
	s_cselect_b64 s[4:5], -1, 0
	s_and_b64 s[2:3], s[4:5], s[2:3]
	v_readlane_b32 s96, v248, 7
	v_readlane_b32 s64, v248, 10
	v_readlane_b32 s30, v248, 5
	s_and_b64 vcc, exec, s[2:3]
	v_readlane_b32 s97, v248, 8
	v_readlane_b32 s61, v248, 2
	v_readlane_b32 s62, v248, 3
	v_readlane_b32 s65, v248, 11
	v_readlane_b32 s31, v248, 6
	s_cbranch_vccz .LBB0_671
	s_load_dwordx2 s[4:5], s[0:1], 0x80
	s_add_i32 s2, s87, 0xa00
	s_lshr_b32 s2, s2, 7
	s_mov_b32 s3, 0
	s_bfe_u32 s8, s87, 0x40003
	s_lshl_b64 s[6:7], s[2:3], 24
	s_waitcnt lgkmcnt(0)
	s_add_u32 s10, s4, s6
	s_addc_u32 s11, s5, s7
	s_add_u32 s18, s90, 0x50000000
	s_addc_u32 s19, s91, 0
	s_lshl_b64 s[4:5], s[2:3], 22
	s_add_u32 s6, s18, s4
	s_addc_u32 s7, s19, s5
	s_lshl_b32 s2, s8, 18
	s_add_u32 s6, s6, s2
	s_mov_b64 s[4:5], s[2:3]
	s_addc_u32 s7, s7, 0
	s_lshl_b32 s2, s87, 8
	s_lshl_b32 s12, s93, 5
	s_and_b32 s13, s2, 0x700
	s_add_i32 s2, s12, s13
	v_lshrrev_b32_e32 v72, 3, v194
	v_or_b32_e32 v66, s2, v72
	s_lshl_b32 s20, s93, 4
	s_lshl_b32 s2, s8, 7
	s_add_i32 s2, s20, s2
	s_lshl_b64 s[8:9], s[2:3], 13
	s_add_u32 s8, s10, s8
	s_addc_u32 s9, s11, s9
	s_lshl_b32 s10, s13, 2
	v_mov_b32_e32 v67, 0
	s_add_u32 s8, s8, s10
	v_lshlrev_b64 v[68:69], 7, v[66:67]
	s_addc_u32 s9, s9, 0
	v_lshlrev_b32_e32 v66, 4, v194
	s_waitcnt vmcnt(2)
	v_lshl_add_u64 v[54:55], s[8:9], 0, v[66:67]
	s_mov_b32 s10, 0x1e000
	v_add_co_u32_e32 v10, vcc, s10, v54
	s_mov_b32 s10, 0x1c000
	s_nop 0
	v_addc_co_u32_e32 v11, vcc, 0, v55, vcc
	v_add_co_u32_e32 v12, vcc, s10, v54
	s_mov_b32 s10, 0x1a000
	s_nop 0
	v_addc_co_u32_e32 v13, vcc, 0, v55, vcc
	v_add_co_u32_e32 v18, vcc, s10, v54
	s_mov_b32 s10, 0x18000
	s_nop 0
	v_addc_co_u32_e32 v19, vcc, 0, v55, vcc
	v_add_co_u32_e32 v20, vcc, s10, v54
	s_mov_b32 s10, 0x16000
	s_nop 0
	v_addc_co_u32_e32 v21, vcc, 0, v55, vcc
	v_add_co_u32_e32 v26, vcc, s10, v54
	s_mov_b32 s10, 0x14000
	s_nop 0
	v_addc_co_u32_e32 v27, vcc, 0, v55, vcc
	v_add_co_u32_e32 v28, vcc, s10, v54
	s_mov_b32 s10, 0x12000
	s_nop 0
	v_addc_co_u32_e32 v29, vcc, 0, v55, vcc
	v_add_co_u32_e32 v34, vcc, s10, v54
	s_mov_b32 s10, 0x10000
	s_nop 0
	v_addc_co_u32_e32 v35, vcc, 0, v55, vcc
	v_add_co_u32_e32 v36, vcc, s10, v54
	s_mov_b32 s10, 0xe000
	s_nop 0
	v_addc_co_u32_e32 v37, vcc, 0, v55, vcc
	s_waitcnt vmcnt(1)
	v_add_co_u32_e32 v42, vcc, s10, v54
	s_mov_b32 s10, 0xc000
	s_nop 0
	v_addc_co_u32_e32 v43, vcc, 0, v55, vcc
	v_add_co_u32_e32 v44, vcc, s10, v54
	s_mov_b32 s10, 0xa000
	s_nop 0
	v_addc_co_u32_e32 v45, vcc, 0, v55, vcc
	s_waitcnt vmcnt(0)
	v_add_co_u32_e32 v50, vcc, s10, v54
	s_mov_b32 s10, 0x8000
	s_nop 0
	v_addc_co_u32_e32 v51, vcc, 0, v55, vcc
	v_add_co_u32_e32 v52, vcc, s10, v54
	s_movk_i32 s10, 0x6000
	s_nop 0
	v_addc_co_u32_e32 v53, vcc, 0, v55, vcc
	v_add_co_u32_e32 v56, vcc, s10, v54
	s_movk_i32 s10, 0x4000
	s_nop 0
	v_addc_co_u32_e32 v57, vcc, 0, v55, vcc
	v_add_co_u32_e32 v62, vcc, s10, v54
	s_movk_i32 s10, 0x2000
	s_nop 0
	v_addc_co_u32_e32 v63, vcc, 0, v55, vcc
	v_add_co_u32_e32 v70, vcc, s10, v54
	global_load_dwordx4 v[2:5], v[10:11], off nt
	global_load_dwordx4 v[6:9], v[12:13], off nt
	v_addc_co_u32_e32 v71, vcc, 0, v55, vcc
	global_load_dwordx4 v[10:13], v[18:19], off nt
	global_load_dwordx4 v[14:17], v[20:21], off nt
	s_nop 0
	global_load_dwordx4 v[18:21], v[26:27], off nt
	global_load_dwordx4 v[22:25], v[28:29], off nt
	s_nop 0
	global_load_dwordx4 v[26:29], v[34:35], off nt
	global_load_dwordx4 v[30:33], v[36:37], off nt
	global_load_dwordx4 v[38:41], v[42:43], off nt
	s_nop 0
	global_load_dwordx4 v[34:37], v[44:45], off nt
	global_load_dwordx4 v[46:49], v[50:51], off nt
	s_nop 0
	global_load_dwordx4 v[42:45], v[52:53], off nt
	global_load_dwordx4 v[58:61], v[56:57], off nt
	s_nop 0
	global_load_dwordx4 v[50:53], v[62:63], off nt
	s_nop 0
	global_load_dwordx4 v[62:65], v[70:71], off nt
	global_load_dwordx4 v[54:57], v66, s[8:9] nt
	v_lshlrev_b32_e32 v66, 4, v0
	v_lshl_add_u64 v[70:71], s[6:7], 0, v[68:69]
	v_and_b32_e32 v68, 0x70, v66
	v_mov_b32_e32 v69, v67
	s_and_b32 s21, s87, 7
	s_and_b32 s22, s87, 15
	v_lshl_add_u64 v[70:71], v[70:71], 0, v[68:69]
	s_mov_b64 s[6:7], s[2:3]
	v_lshlrev_b32_e32 v66, 2, v194
	v_or_b32_e32 v75, s12, v72
	s_add_u32 s23, s90, 0x30000000
	s_movk_i32 s2, 0x90
	v_mul_u32_u24_e32 v74, 0x240, v194
	s_addc_u32 s24, s91, 0
	v_mul_lo_u32 v76, v75, s2
	s_add_i32 s25, s87, 0x2a80
	s_mov_b32 s26, 0xc3e00000
	v_lshlrev_b32_e32 v66, 2, v66
	v_mov_b32_e32 v77, 0x43e00000
	s_mov_b32 s27, 0
	v_mov_b64_e32 v[72:73], v[70:71]
	s_waitcnt vmcnt(0)
	s_branch .LBB0_665

; #define LAS __attribute__((address_space(3)))
; __device__ __forceinline__ void conv8b_run(const Ctx& X, int first, int step, int count) {
;     ...
;         LAS uchar* buf = X.lds + (j & 1) * CVT_BUF;
; #pragma unroll
;         for (int q = 0; q < 4; ++q) { u32x4 o;
;             o.x = pk_fp8x4(v[0][q] * W8_SCALE, v[1][q] * W8_SCALE, v[2][q] * W8_SCALE, v[3][q] * W8_SCALE); o.y = pk_fp8x4(v[4][q] * W8_SCALE, v[5][q] * W8_SCALE, v[6][q] * W8_SCALE, v[7][q] * W8_SCALE);
;             o.z = pk_fp8x4(v[8][q] * W8_SCALE, v[9][q] * W8_SCALE, v[10][q] * W8_SCALE, v[11][q] * W8_SCALE); o.w = pk_fp8x4(v[12][q] * W8_SCALE, v[13][q] * W8_SCALE, v[14][q] * W8_SCALE, v[15][q] * W8_SCALE);
;             *(LAS u32x4*)(buf + (4 * X.lane + q) * CVT_STRIDE + 16 * X.wave) = o; }
;         if (j + 1 < count) { cn = conv8b_dec(X, first + (j + 1) * step);
; #pragma unroll
;             for (int i = 0; i < 16; ++i) v[i] = __builtin_nontemporal_load((const f32x4*)(cn.W + (size_t)i * cn.N)); }
.LBB0_665:
	s_waitcnt vmcnt(4)
	v_mul_f32_e32 v78, 0x42800000, v54
	v_mul_f32_e32 v79, 0x42800000, v62
	v_med3_f32 v81, v78, s26, v77
	v_med3_f32 v79, v79, s26, v77
	v_mov_b32_e32 v78, 0
	v_cvt_pk_fp8_f32 v78, v81, v79
	v_mul_f32_e32 v80, 0x42800000, v50
	v_mul_f32_e32 v79, 0x42800000, v58
	v_med3_f32 v80, v80, s26, v77
	v_med3_f32 v79, v79, s26, v77
	v_cvt_pk_fp8_f32 v78, v80, v79 op_sel:[0,0,1]
	v_mul_f32_e32 v79, 0x42800000, v42
	v_mul_f32_e32 v80, 0x42800000, v46
	v_med3_f32 v82, v79, s26, v77
	v_med3_f32 v80, v80, s26, v77
	v_mov_b32_e32 v79, 0
	v_cvt_pk_fp8_f32 v79, v82, v80
	v_mul_f32_e32 v81, 0x42800000, v34
	v_mul_f32_e32 v80, 0x42800000, v38
	v_med3_f32 v81, v81, s26, v77
	v_med3_f32 v80, v80, s26, v77
	v_cvt_pk_fp8_f32 v79, v81, v80 op_sel:[0,0,1]
	v_mul_f32_e32 v80, 0x42800000, v30
	v_mul_f32_e32 v81, 0x42800000, v26
	v_med3_f32 v83, v80, s26, v77
	v_med3_f32 v81, v81, s26, v77
	v_mov_b32_e32 v80, 0
	v_cvt_pk_fp8_f32 v80, v83, v81
	v_mul_f32_e32 v82, 0x42800000, v22
	v_mul_f32_e32 v81, 0x42800000, v18
	v_med3_f32 v82, v82, s26, v77
	v_med3_f32 v81, v81, s26, v77
	v_cvt_pk_fp8_f32 v80, v82, v81 op_sel:[0,0,1]
	v_mul_f32_e32 v81, 0x42800000, v14
	v_mul_f32_e32 v82, 0x42800000, v10
	v_med3_f32 v84, v81, s26, v77
	v_med3_f32 v82, v82, s26, v77
	v_mov_b32_e32 v81, 0
	v_cvt_pk_fp8_f32 v81, v84, v82
	v_mul_f32_e32 v83, 0x42800000, v6
	v_mul_f32_e32 v82, 0x42800000, v2
	s_bitcmp1_b32 s27, 0
	v_med3_f32 v83, v83, s26, v77
	v_med3_f32 v82, v82, s26, v77
	s_cselect_b32 s2, 0x9000, 0
	v_cvt_pk_fp8_f32 v81, v83, v82 op_sel:[0,0,1]
	s_add_i32 s28, s2, 0
	s_add_i32 s2, s20, s28
	v_add_u32_e32 v90, s2, v74
	ds_write_b128 v90, v[78:81]
	v_mul_f32_e32 v78, 0x42800000, v55
	v_mul_f32_e32 v79, 0x42800000, v63
	v_med3_f32 v81, v78, s26, v77
	v_med3_f32 v79, v79, s26, v77
	v_mov_b32_e32 v78, 0
	v_cvt_pk_fp8_f32 v78, v81, v79
	v_mul_f32_e32 v80, 0x42800000, v51
	v_mul_f32_e32 v79, 0x42800000, v59
	v_med3_f32 v80, v80, s26, v77
	v_med3_f32 v79, v79, s26, v77
	v_cvt_pk_fp8_f32 v78, v80, v79 op_sel:[0,0,1]
	v_mul_f32_e32 v79, 0x42800000, v43
	v_mul_f32_e32 v80, 0x42800000, v47
	v_med3_f32 v82, v79, s26, v77
	v_med3_f32 v80, v80, s26, v77
	v_mov_b32_e32 v79, 0
	v_cvt_pk_fp8_f32 v79, v82, v80
	v_mul_f32_e32 v81, 0x42800000, v35
	v_mul_f32_e32 v80, 0x42800000, v39
	v_med3_f32 v81, v81, s26, v77
	v_med3_f32 v80, v80, s26, v77
	v_cvt_pk_fp8_f32 v79, v81, v80 op_sel:[0,0,1]
	v_mul_f32_e32 v80, 0x42800000, v31
	v_mul_f32_e32 v81, 0x42800000, v27
	v_med3_f32 v83, v80, s26, v77
	v_med3_f32 v81, v81, s26, v77
	v_mov_b32_e32 v80, 0
	v_cvt_pk_fp8_f32 v80, v83, v81
	v_mul_f32_e32 v82, 0x42800000, v23
	v_mul_f32_e32 v81, 0x42800000, v19
	v_med3_f32 v82, v82, s26, v77
	v_med3_f32 v81, v81, s26, v77
	v_cvt_pk_fp8_f32 v80, v82, v81 op_sel:[0,0,1]
	v_mul_f32_e32 v81, 0x42800000, v15
	v_mul_f32_e32 v82, 0x42800000, v11
	v_med3_f32 v84, v81, s26, v77
	v_med3_f32 v82, v82, s26, v77
	v_mov_b32_e32 v81, 0
	v_cvt_pk_fp8_f32 v81, v84, v82
	v_mul_f32_e32 v83, 0x42800000, v7
	v_mul_f32_e32 v82, 0x42800000, v3
	v_med3_f32 v83, v83, s26, v77
	v_med3_f32 v82, v82, s26, v77
	v_cvt_pk_fp8_f32 v81, v83, v82 op_sel:[0,0,1]
	v_mul_f32_e32 v82, 0x42800000, v56
	v_mul_f32_e32 v83, 0x42800000, v64
	v_med3_f32 v85, v82, s26, v77
	v_med3_f32 v83, v83, s26, v77
	v_mov_b32_e32 v82, 0
	v_cvt_pk_fp8_f32 v82, v85, v83
	v_mul_f32_e32 v84, 0x42800000, v52
	v_mul_f32_e32 v83, 0x42800000, v60
	v_med3_f32 v84, v84, s26, v77
	v_med3_f32 v83, v83, s26, v77
	v_cvt_pk_fp8_f32 v82, v84, v83 op_sel:[0,0,1]
	v_mul_f32_e32 v83, 0x42800000, v44
	v_mul_f32_e32 v84, 0x42800000, v48
	v_med3_f32 v86, v83, s26, v77
	v_med3_f32 v84, v84, s26, v77
	v_mov_b32_e32 v83, 0
	v_cvt_pk_fp8_f32 v83, v86, v84
	v_mul_f32_e32 v85, 0x42800000, v36
	v_mul_f32_e32 v84, 0x42800000, v40
	v_med3_f32 v85, v85, s26, v77
	v_med3_f32 v84, v84, s26, v77
	v_cvt_pk_fp8_f32 v83, v85, v84 op_sel:[0,0,1]
	v_mul_f32_e32 v84, 0x42800000, v32
	v_mul_f32_e32 v85, 0x42800000, v28
	v_med3_f32 v87, v84, s26, v77
	v_med3_f32 v85, v85, s26, v77
	v_mov_b32_e32 v84, 0
	v_cvt_pk_fp8_f32 v84, v87, v85
	v_mul_f32_e32 v86, 0x42800000, v24
	v_mul_f32_e32 v85, 0x42800000, v20
	v_med3_f32 v86, v86, s26, v77
	v_med3_f32 v85, v85, s26, v77
	v_cvt_pk_fp8_f32 v84, v86, v85 op_sel:[0,0,1]
	v_mul_f32_e32 v85, 0x42800000, v16
	v_mul_f32_e32 v86, 0x42800000, v12
	v_med3_f32 v88, v85, s26, v77
	v_med3_f32 v86, v86, s26, v77
	v_mov_b32_e32 v85, 0
	v_cvt_pk_fp8_f32 v85, v88, v86
	v_mul_f32_e32 v87, 0x42800000, v8
	v_mul_f32_e32 v86, 0x42800000, v4
	v_med3_f32 v87, v87, s26, v77
	v_med3_f32 v86, v86, s26, v77
	v_cvt_pk_fp8_f32 v85, v87, v86 op_sel:[0,0,1]
	v_mul_f32_e32 v86, 0x42800000, v57
	v_mul_f32_e32 v87, 0x42800000, v65
	v_med3_f32 v89, v86, s26, v77
	v_med3_f32 v87, v87, s26, v77
	v_mov_b32_e32 v86, 0
	v_cvt_pk_fp8_f32 v86, v89, v87
	v_mul_f32_e32 v88, 0x42800000, v53
	v_mul_f32_e32 v87, 0x42800000, v61
	v_med3_f32 v88, v88, s26, v77
	v_med3_f32 v87, v87, s26, v77
	v_cvt_pk_fp8_f32 v86, v88, v87 op_sel:[0,0,1]
	v_mul_f32_e32 v87, 0x42800000, v45
	v_mul_f32_e32 v88, 0x42800000, v49
	v_med3_f32 v91, v87, s26, v77
	v_med3_f32 v88, v88, s26, v77
	v_mov_b32_e32 v87, 0
	v_cvt_pk_fp8_f32 v87, v91, v88
	v_mul_f32_e32 v89, 0x42800000, v37
	v_mul_f32_e32 v88, 0x42800000, v41
	v_med3_f32 v89, v89, s26, v77
	v_med3_f32 v88, v88, s26, v77
	v_cvt_pk_fp8_f32 v87, v89, v88 op_sel:[0,0,1]
	v_mul_f32_e32 v88, 0x42800000, v33
	v_mul_f32_e32 v89, 0x42800000, v29
	v_med3_f32 v92, v88, s26, v77
	v_med3_f32 v89, v89, s26, v77
	v_mov_b32_e32 v88, 0
	v_cvt_pk_fp8_f32 v88, v92, v89
	v_mul_f32_e32 v91, 0x42800000, v25
	v_mul_f32_e32 v89, 0x42800000, v21
	v_med3_f32 v91, v91, s26, v77
	v_med3_f32 v89, v89, s26, v77
	v_cvt_pk_fp8_f32 v88, v91, v89 op_sel:[0,0,1]
	v_mul_f32_e32 v89, 0x42800000, v17
	v_mul_f32_e32 v91, 0x42800000, v13
	v_med3_f32 v93, v89, s26, v77
	v_med3_f32 v91, v91, s26, v77
	v_mov_b32_e32 v89, 0
	v_cvt_pk_fp8_f32 v89, v93, v91
	v_mul_f32_e32 v92, 0x42800000, v9
	v_mul_f32_e32 v91, 0x42800000, v5
	v_med3_f32 v92, v92, s26, v77
	v_med3_f32 v91, v91, s26, v77
	v_cvt_pk_fp8_f32 v89, v92, v91 op_sel:[0,0,1]
	s_cmp_gt_u32 s27, 9
	ds_write_b128 v90, v[78:81] offset:144
	ds_write_b128 v90, v[82:85] offset:288
	ds_write_b128 v90, v[86:89] offset:432
	s_cbranch_scc1 .LBB0_664
	s_cmpk_gt_i32 s25, 0x1fff
	s_mov_b64 s[14:15], -1
	s_cbranch_scc0 .LBB0_668
	s_load_dwordx2 s[8:9], s[0:1], 0x80
	s_add_i32 s2, s25, 0xffffe000
	s_lshr_b32 s2, s2, 7
	s_lshl_b64 s[10:11], s[2:3], 24
	s_mov_b64 s[14:15], 0
	s_waitcnt lgkmcnt(0)
	s_add_u32 s8, s8, s10
	s_addc_u32 s9, s9, s11
	s_lshl_b64 s[10:11], s[2:3], 22
	s_add_u32 s10, s18, s10
	s_addc_u32 s11, s19, s11
